# v12 + nt on B-operand LDS-DMA loads in MoE gate/up GEMM loops
# baseline (speedup 1.0000x reference)
; __device__ __forceinline__ unsigned cvt_pk_bf16(float lo, float hi) { unsigned r; asm volatile("v_cvt_pk_bf16_f32 %0, %1, %2" : "=v"(r) : "v"(lo), "v"(hi)); return r; }
; #define PG8_STAGE(bufoff, gbase, v0, v1) do { \
;         __builtin_amdgcn_global_load_lds((const unsigned*)((const char*)(gbase) + (v0)), (LAS unsigned*)(lds + (bufoff) + ldsw), 16, 0, 0); \
;         __builtin_amdgcn_global_load_lds((const unsigned*)((const char*)(gbase) + (v1)), (LAS unsigned*)(lds + (bufoff) + ldsw + 8192), 16, 0, 0); } while (0)
; #define PG8_LDA(dst, b, h) do { _Pragma("unroll") for (int m = 0; m < 4; ++m) _Pragma("unroll") for (int k = 0; k < 2; ++k) dst[m][k] = *(const LAS bf16x8*)(lds + PG8_SA(b, h) + aoff + m * 2048 + k * 1024); } while (0)
; #define PG8_WAIT_V(n) asm volatile("s_waitcnt vmcnt(" #n ")" ::: "memory")
; #define PG8_WAIT_L(n) asm volatile("s_waitcnt lgkmcnt(" #n ")" ::: "memory")
; template <class Epi, class Sched>
; __device__ __forceinline__ void gemm_phase(LAS unsigned char* lds, const int K, const Sched& S, const Epi& E) {
;     ...
;             PG8_LDB(B0, 0, 0); PG8_SCHED; PG8_LDA(At, 0, 0); PG8_STAGE(PG8_SA(1, 1), a1, c10, c11);
;             PG8_WAIT_L(8); PG8_BAR; PG8_WAIT_L(0); PG8_MMA(0, 0, At, B0); PG8_BAR; PG8_SCHED;
;             PG8_LDB(B1, 0, 1); PG8_STAGE(PG8_SB(0, 0), b2, voffB0, voffB1);
;             PG8_BAR; PG8_WAIT_L(0); PG8_MMA(0, 1, At, B1); PG8_BAR;
;             PG8_LDA(At, 0, 1); PG8_STAGE(PG8_SA(0, 0), a2, x00, x01);
;             PG8_BAR; PG8_WAIT_L(0); PG8_MMA(1, 0, At, B0); PG8_BAR; PG8_SCHED;
;             PG8_STAGE(PG8_SB(0, 1), b2 + hstep, voffB0, voffB1);
;             PG8_WAIT_V(6); PG8_BAR; PG8_MMA(1, 1, At, B1); PG8_BAR;
; template <int BANK, int WAITN> __device__ __forceinline__ void bg_finish1(BgState& b) {
;     ...
;     if (dst != nullptr) {
; #pragma unroll
;         for (int c = 0; c < 4; ++c) { u32x4 w;
;             w.x = cvt_pk_bf16(b.r[(BANK * 8 + 0) * 4 + c], b.r[(BANK * 8 + 1) * 4 + c]); w.y = cvt_pk_bf16(b.r[(BANK * 8 + 2) * 4 + c], b.r[(BANK * 8 + 3) * 4 + c]);
;             w.z = cvt_pk_bf16(b.r[(BANK * 8 + 4) * 4 + c], b.r[(BANK * 8 + 5) * 4 + c]); w.w = cvt_pk_bf16(b.r[(BANK * 8 + 6) * 4 + c], b.r[(BANK * 8 + 7) * 4 + c]);
;             bf16_t* dp = dst + (c & 1) * 512 + (c >> 1) * b.o2[BANK];
;             asm volatile("global_store_dwordx4 %0, %1, off\n\ts_nop 1" :: "v"(dp), "v"(w) : "memory"); }
.LBB0_1094:
	v_add_u32_e32 v139, s46, v149
	s_add_u32 s22, s0, s20
	ds_read_b128 v[160:163], v139
	ds_read_b128 v[164:167], v139 offset:1024
	ds_read_b128 v[168:171], v139 offset:2048
	ds_read_b128 v[172:175], v139 offset:3072
	s_addc_u32 s23, s1, s21
	s_add_u32 s24, s22, 0x34c30100
	s_addc_u32 s25, s23, 0
	s_cmpk_eq_i32 s20, 0xf00
	s_cselect_b64 vcc, -1, 0
	s_and_b64 s[22:23], vcc, exec
	v_cndmask_b32_e32 v134, v158, v156, vcc
	s_cselect_b32 s27, s3, s25
	s_cselect_b32 s26, s2, s24
	v_cndmask_b32_e32 v139, v138, v154, vcc
	s_cselect_b32 s23, s19, s15
	s_cselect_b32 s22, s18, s13
	v_cndmask_b32_e32 v204, v136, v155, vcc
	s_add_u32 s24, s22, 0x20000
	s_addc_u32 s25, s23, 0
	v_lshl_add_u64 v[206:207], v[144:145], 0, s[20:21]
	s_add_i32 m0, s37, 0xc000
	ds_read_b128 v[176:179], v151
	ds_read_b128 v[180:183], v151 offset:1024
	ds_read_b128 v[184:187], v151 offset:2048
	ds_read_b128 v[188:191], v151 offset:3072
	ds_read_b128 v[192:195], v151 offset:4096
	ds_read_b128 v[196:199], v151 offset:5120
	ds_read_b128 v[200:203], v151 offset:6144
	ds_read_b128 v[208:211], v151 offset:7168
	global_load_lds_dwordx4 v[206:207], off
	v_lshl_add_u64 v[206:207], v[142:143], 0, s[20:21]
	s_add_i32 m0, s37, 0xe000
	s_nop 0
	global_load_lds_dwordx4 v[206:207], off
	s_waitcnt lgkmcnt(8)
	s_barrier
	s_waitcnt lgkmcnt(0)
	s_setprio 1
	s_waitcnt lgkmcnt(0)
	v_mfma_f32_16x16x32_bf16 v[126:129], v[160:163], v[176:179], v[126:129]
	v_mfma_f32_16x16x32_bf16 v[122:125], v[168:171], v[176:179], v[122:125]
	v_mfma_f32_16x16x32_bf16 v[110:113], v[160:163], v[184:187], v[110:113]
	v_mfma_f32_16x16x32_bf16 v[106:109], v[168:171], v[184:187], v[106:109]
	v_mfma_f32_16x16x32_bf16 v[94:97], v[160:163], v[192:195], v[94:97]
	v_mfma_f32_16x16x32_bf16 v[90:93], v[168:171], v[192:195], v[90:93]
	v_mfma_f32_16x16x32_bf16 v[78:81], v[160:163], v[200:203], v[78:81]
	v_mfma_f32_16x16x32_bf16 v[74:77], v[168:171], v[200:203], v[74:77]
	v_mfma_f32_16x16x32_bf16 v[126:129], v[164:167], v[180:183], v[126:129]
	v_mfma_f32_16x16x32_bf16 v[122:125], v[172:175], v[180:183], v[122:125]
	v_mfma_f32_16x16x32_bf16 v[110:113], v[164:167], v[188:191], v[110:113]
	v_mfma_f32_16x16x32_bf16 v[106:109], v[172:175], v[188:191], v[106:109]
	v_mfma_f32_16x16x32_bf16 v[94:97], v[164:167], v[196:199], v[94:97]
	v_mfma_f32_16x16x32_bf16 v[90:93], v[172:175], v[196:199], v[90:93]
	v_mfma_f32_16x16x32_bf16 v[78:81], v[164:167], v[208:211], v[78:81]
	v_mfma_f32_16x16x32_bf16 v[74:77], v[172:175], v[208:211], v[74:77]
	s_setprio 0
	s_barrier
	s_add_i32 s55, s46, s36
	v_add_u32_e32 v141, s48, v149
	v_lshl_add_u64 v[206:207], s[22:23], 0, v[130:131]
	s_mov_b32 m0, s55
	ds_read_b128 v[212:215], v141
	ds_read_b128 v[216:219], v141 offset:1024
	ds_read_b128 v[220:223], v141 offset:2048
	ds_read_b128 v[224:227], v141 offset:3072
	global_load_lds_dwordx4 v[206:207], off nt
	v_lshl_add_u64 v[228:229], s[22:23], 0, v[132:133]
	s_add_i32 m0, s55, 0x2000
	s_nop 0
	global_load_lds_dwordx4 v[228:229], off nt
	s_barrier
	s_waitcnt lgkmcnt(0)
	s_setprio 1
	s_waitcnt lgkmcnt(0)
	v_mfma_f32_16x16x32_bf16 v[118:121], v[212:215], v[176:179], v[118:121]
	v_mfma_f32_16x16x32_bf16 v[114:117], v[220:223], v[176:179], v[114:117]
	v_mfma_f32_16x16x32_bf16 v[102:105], v[212:215], v[184:187], v[102:105]
	v_mfma_f32_16x16x32_bf16 v[98:101], v[220:223], v[184:187], v[98:101]
	v_mfma_f32_16x16x32_bf16 v[86:89], v[212:215], v[192:195], v[86:89]
	v_mfma_f32_16x16x32_bf16 v[82:85], v[220:223], v[192:195], v[82:85]
	v_mfma_f32_16x16x32_bf16 v[70:73], v[212:215], v[200:203], v[70:73]
	v_mfma_f32_16x16x32_bf16 v[66:69], v[220:223], v[200:203], v[66:69]
	v_mfma_f32_16x16x32_bf16 v[118:121], v[216:219], v[180:183], v[118:121]
	v_mfma_f32_16x16x32_bf16 v[114:117], v[224:227], v[180:183], v[114:117]
	v_mfma_f32_16x16x32_bf16 v[102:105], v[216:219], v[188:191], v[102:105]
	v_mfma_f32_16x16x32_bf16 v[98:101], v[224:227], v[188:191], v[98:101]
	v_mfma_f32_16x16x32_bf16 v[86:89], v[216:219], v[196:199], v[86:89]
	v_mfma_f32_16x16x32_bf16 v[82:85], v[224:227], v[196:199], v[82:85]
	v_mfma_f32_16x16x32_bf16 v[70:73], v[216:219], v[208:211], v[70:73]
	v_mfma_f32_16x16x32_bf16 v[66:69], v[224:227], v[208:211], v[66:69]
	s_setprio 0
	s_mov_b32 m0, s37
	s_barrier
	ds_read_b128 v[176:179], v151 offset:16384
	ds_read_b128 v[180:183], v151 offset:17408
	ds_read_b128 v[184:187], v151 offset:18432
	ds_read_b128 v[188:191], v151 offset:19456
	ds_read_b128 v[192:195], v151 offset:20480
	ds_read_b128 v[196:199], v151 offset:21504
	ds_read_b128 v[200:203], v151 offset:22528
	ds_read_b128 v[208:211], v151 offset:23552
	global_load_lds_dwordx4 v134, s[26:27]
	s_mov_b32 m0, s38
	v_mov_b32_e32 v205, v135
	global_load_lds_dwordx4 v204, s[26:27]
	s_barrier
	s_waitcnt lgkmcnt(0)
	v_lshl_add_u64 v[230:231], s[26:27], 0, v[134:135]
	v_lshl_add_u64 v[204:205], s[26:27], 0, v[204:205]
	s_setprio 1
	s_waitcnt lgkmcnt(0)
	v_mfma_f32_16x16x32_bf16 v[62:65], v[160:163], v[176:179], v[62:65]
	v_mfma_f32_16x16x32_bf16 v[58:61], v[168:171], v[176:179], v[58:61]
	v_mfma_f32_16x16x32_bf16 v[46:49], v[160:163], v[184:187], v[46:49]
	v_mfma_f32_16x16x32_bf16 v[42:45], v[168:171], v[184:187], v[42:45]
	v_mfma_f32_16x16x32_bf16 v[30:33], v[160:163], v[192:195], v[30:33]
	v_mfma_f32_16x16x32_bf16 v[26:29], v[168:171], v[192:195], v[26:29]
	v_mfma_f32_16x16x32_bf16 v[14:17], v[160:163], v[200:203], v[14:17]
	v_mfma_f32_16x16x32_bf16 v[10:13], v[168:171], v[200:203], v[10:13]
	v_mfma_f32_16x16x32_bf16 v[62:65], v[164:167], v[180:183], v[62:65]
	v_mfma_f32_16x16x32_bf16 v[58:61], v[172:175], v[180:183], v[58:61]
	v_mfma_f32_16x16x32_bf16 v[46:49], v[164:167], v[188:191], v[46:49]
	v_mfma_f32_16x16x32_bf16 v[42:45], v[172:175], v[188:191], v[42:45]
	v_mfma_f32_16x16x32_bf16 v[30:33], v[164:167], v[196:199], v[30:33]
	v_mfma_f32_16x16x32_bf16 v[26:29], v[172:175], v[196:199], v[26:29]
	v_mfma_f32_16x16x32_bf16 v[14:17], v[164:167], v[208:211], v[14:17]
	v_mfma_f32_16x16x32_bf16 v[10:13], v[172:175], v[208:211], v[10:13]
	s_setprio 0
	s_barrier
	s_add_i32 s55, s48, s36
	v_lshl_add_u64 v[160:161], v[206:207], 0, s[4:5]
	s_mov_b32 m0, s55
	s_nop 0
	global_load_lds_dwordx4 v[160:161], off nt
	v_lshl_add_u64 v[160:161], v[228:229], 0, s[4:5]
	s_add_i32 m0, s55, 0x2000
	s_nop 0
	global_load_lds_dwordx4 v[160:161], off nt
	s_cmp_eq_u32 s82, 0
	s_cbranch_scc1 .Lpb8_p4n
	s_waitcnt vmcnt(14)
	v_cvt_pk_bf16_f32 v244, v244, v245
	v_cvt_pk_bf16_f32 v245, v246, v247
	v_cvt_pk_bf16_f32 v246, v248, v249
	v_cvt_pk_bf16_f32 v247, v250, v251
	global_store_dwordx4 v253, v[244:247], s[78:79] nt
	s_mov_b32 s82, 0
	s_waitcnt vmcnt(7)
	s_branch .Lpb8_p4j

; #define PG8_STAGE(bufoff, gbase, v0, v1) do { \
;         __builtin_amdgcn_global_load_lds((const unsigned*)((const char*)(gbase) + (v0)), (LAS unsigned*)(lds + (bufoff) + ldsw), 16, 0, 0); \
;         __builtin_amdgcn_global_load_lds((const unsigned*)((const char*)(gbase) + (v1)), (LAS unsigned*)(lds + (bufoff) + ldsw + 8192), 16, 0, 0); } while (0)
; #define PG8_LDA(dst, b, h) do { _Pragma("unroll") for (int m = 0; m < 4; ++m) _Pragma("unroll") for (int k = 0; k < 2; ++k) dst[m][k] = *(const LAS bf16x8*)(lds + PG8_SA(b, h) + aoff + m * 2048 + k * 1024); } while (0)
; #define PG8_LDB(dst, b, h) do { _Pragma("unroll") for (int n = 0; n < 2; ++n) _Pragma("unroll") for (int k = 0; k < 2; ++k) dst[n][k] = *(const LAS bf16x8*)(lds + PG8_SB(b, h) + boff + n * 2048 + k * 1024); } while (0)
; #define PG8_MMA(ai, bj, At, Bt) do { __builtin_amdgcn_s_setprio(1); _Pragma("unroll") for (int m = 0; m < 4; ++m) _Pragma("unroll") for (int n = 0; n < 2; ++n) _Pragma("unroll") for (int k = 0; k < 2; ++k) \
;         acc[ai][bj][m][n] = __builtin_amdgcn_mfma_f32_16x16x32_bf16(Bt[n][k], At[m][k], acc[ai][bj][m][n], 0, 0, 0); __builtin_amdgcn_s_setprio(0); } while (0)
; #define PG8_WAIT_V(n) asm volatile("s_waitcnt vmcnt(" #n ")" ::: "memory")
; #define PG8_WAIT_L(n) asm volatile("s_waitcnt lgkmcnt(" #n ")" ::: "memory")
; #define PG8_BAR __builtin_amdgcn_s_barrier()
; #define PG8_SCHED __builtin_amdgcn_sched_barrier(0)
; template <class Epi, class Sched>
; __device__ __forceinline__ void gemm_phase(LAS unsigned char* lds, const int K, const Sched& S, const Epi& E) {
;     ...
;             PG8_WAIT_L(8); PG8_BAR; PG8_WAIT_L(0); PG8_MMA(0, 0, At, B0); PG8_BAR; PG8_SCHED;
;             PG8_LDB(B1, 1, 1); PG8_STAGE(PG8_SB(1, 0), b3, voffB0, voffB1);
;             PG8_BAR; PG8_WAIT_L(0); PG8_MMA(0, 1, At, B1); PG8_BAR;
;             PG8_LDA(At, 1, 1); PG8_STAGE(PG8_SA(1, 0), a3, x00, x01);
;             PG8_BAR; PG8_WAIT_L(0); PG8_MMA(1, 0, At, B0); PG8_BAR; PG8_SCHED;
;             PG8_STAGE(PG8_SB(1, 1), b3 + hstep, voffB0, voffB1);
;             PG8_WAIT_V(6); PG8_BAR; PG8_MMA(1, 1, At, B1); PG8_BAR;
.Lpb8_p5n:
	s_waitcnt lgkmcnt(8)
	s_barrier
	s_waitcnt lgkmcnt(0)
	s_setprio 1
	s_waitcnt lgkmcnt(0)
	v_mfma_f32_16x16x32_bf16 v[126:129], v[160:163], v[176:179], v[126:129]
	v_mfma_f32_16x16x32_bf16 v[122:125], v[168:171], v[176:179], v[122:125]
	v_mfma_f32_16x16x32_bf16 v[110:113], v[160:163], v[184:187], v[110:113]
	v_mfma_f32_16x16x32_bf16 v[106:109], v[168:171], v[184:187], v[106:109]
	v_mfma_f32_16x16x32_bf16 v[94:97], v[160:163], v[192:195], v[94:97]
	v_mfma_f32_16x16x32_bf16 v[90:93], v[168:171], v[192:195], v[90:93]
	v_mfma_f32_16x16x32_bf16 v[78:81], v[160:163], v[200:203], v[78:81]
	v_mfma_f32_16x16x32_bf16 v[74:77], v[168:171], v[200:203], v[74:77]
	v_mfma_f32_16x16x32_bf16 v[126:129], v[164:167], v[180:183], v[126:129]
	v_mfma_f32_16x16x32_bf16 v[122:125], v[172:175], v[180:183], v[122:125]
	v_mfma_f32_16x16x32_bf16 v[110:113], v[164:167], v[188:191], v[110:113]
	v_mfma_f32_16x16x32_bf16 v[106:109], v[172:175], v[188:191], v[106:109]
	v_mfma_f32_16x16x32_bf16 v[94:97], v[164:167], v[196:199], v[94:97]
	v_mfma_f32_16x16x32_bf16 v[90:93], v[172:175], v[196:199], v[90:93]
	v_mfma_f32_16x16x32_bf16 v[78:81], v[164:167], v[208:211], v[78:81]
	v_mfma_f32_16x16x32_bf16 v[74:77], v[172:175], v[208:211], v[74:77]
	s_setprio 0
	s_barrier
	s_add_i32 s26, 0, 0x1c000
	s_add_i32 s27, s55, s36
	v_add_u32_e32 v134, s26, v149
	v_lshl_add_u64 v[206:207], s[24:25], 0, v[130:131]
	s_mov_b32 m0, s27
	ds_read_b128 v[212:215], v134
	ds_read_b128 v[216:219], v134 offset:1024
	ds_read_b128 v[220:223], v134 offset:2048
	ds_read_b128 v[224:227], v134 offset:3072
	global_load_lds_dwordx4 v[206:207], off nt
	v_lshl_add_u64 v[206:207], s[24:25], 0, v[132:133]
	s_add_i32 m0, s27, 0x2000
	s_nop 0
	global_load_lds_dwordx4 v[206:207], off nt
	s_barrier
	s_waitcnt lgkmcnt(0)
	s_setprio 1
	s_waitcnt lgkmcnt(0)
	v_mfma_f32_16x16x32_bf16 v[118:121], v[212:215], v[176:179], v[118:121]
	v_mfma_f32_16x16x32_bf16 v[114:117], v[220:223], v[176:179], v[114:117]
	v_mfma_f32_16x16x32_bf16 v[102:105], v[212:215], v[184:187], v[102:105]
	v_mfma_f32_16x16x32_bf16 v[98:101], v[220:223], v[184:187], v[98:101]
	v_mfma_f32_16x16x32_bf16 v[86:89], v[212:215], v[192:195], v[86:89]
	v_mfma_f32_16x16x32_bf16 v[82:85], v[220:223], v[192:195], v[82:85]
	v_mfma_f32_16x16x32_bf16 v[70:73], v[212:215], v[200:203], v[70:73]
	v_mfma_f32_16x16x32_bf16 v[66:69], v[220:223], v[200:203], v[66:69]
	v_mfma_f32_16x16x32_bf16 v[118:121], v[216:219], v[180:183], v[118:121]
	v_mfma_f32_16x16x32_bf16 v[114:117], v[224:227], v[180:183], v[114:117]
	v_mfma_f32_16x16x32_bf16 v[102:105], v[216:219], v[188:191], v[102:105]
	v_mfma_f32_16x16x32_bf16 v[98:101], v[224:227], v[188:191], v[98:101]
	v_mfma_f32_16x16x32_bf16 v[86:89], v[216:219], v[196:199], v[86:89]
	v_mfma_f32_16x16x32_bf16 v[82:85], v[224:227], v[196:199], v[82:85]
	v_mfma_f32_16x16x32_bf16 v[70:73], v[216:219], v[208:211], v[70:73]
	v_mfma_f32_16x16x32_bf16 v[66:69], v[224:227], v[208:211], v[66:69]
	s_setprio 0
	s_mov_b32 m0, s43
	v_lshl_add_u64 v[206:207], v[230:231], 0, s[10:11]
	s_barrier
	ds_read_b128 v[176:179], v151 offset:49152
	ds_read_b128 v[180:183], v151 offset:50176
	ds_read_b128 v[184:187], v151 offset:51200
	ds_read_b128 v[188:191], v151 offset:52224
	ds_read_b128 v[192:195], v151 offset:53248
	ds_read_b128 v[196:199], v151 offset:54272
	ds_read_b128 v[200:203], v151 offset:55296
	ds_read_b128 v[208:211], v151 offset:56320
	global_load_lds_dwordx4 v[206:207], off
	v_lshl_add_u64 v[204:205], v[204:205], 0, s[10:11]
	s_mov_b32 m0, s44
	s_nop 0
	global_load_lds_dwordx4 v[204:205], off
	s_barrier
	s_waitcnt lgkmcnt(0)
	s_setprio 1
	s_waitcnt lgkmcnt(0)
	v_mfma_f32_16x16x32_bf16 v[62:65], v[160:163], v[176:179], v[62:65]
	v_mfma_f32_16x16x32_bf16 v[58:61], v[168:171], v[176:179], v[58:61]
	v_mfma_f32_16x16x32_bf16 v[46:49], v[160:163], v[184:187], v[46:49]
	v_mfma_f32_16x16x32_bf16 v[42:45], v[168:171], v[184:187], v[42:45]
	v_mfma_f32_16x16x32_bf16 v[30:33], v[160:163], v[192:195], v[30:33]
	v_mfma_f32_16x16x32_bf16 v[26:29], v[168:171], v[192:195], v[26:29]
	v_mfma_f32_16x16x32_bf16 v[14:17], v[160:163], v[200:203], v[14:17]
	v_mfma_f32_16x16x32_bf16 v[10:13], v[168:171], v[200:203], v[10:13]
	v_mfma_f32_16x16x32_bf16 v[62:65], v[164:167], v[180:183], v[62:65]
	v_mfma_f32_16x16x32_bf16 v[58:61], v[172:175], v[180:183], v[58:61]
	v_mfma_f32_16x16x32_bf16 v[46:49], v[164:167], v[188:191], v[46:49]
	v_mfma_f32_16x16x32_bf16 v[42:45], v[172:175], v[188:191], v[42:45]
	v_mfma_f32_16x16x32_bf16 v[30:33], v[164:167], v[196:199], v[30:33]
	v_mfma_f32_16x16x32_bf16 v[26:29], v[172:175], v[196:199], v[26:29]
	v_mfma_f32_16x16x32_bf16 v[14:17], v[164:167], v[208:211], v[14:17]
	v_mfma_f32_16x16x32_bf16 v[10:13], v[172:175], v[208:211], v[10:13]
	s_setprio 0
	s_barrier
	s_add_u32 s22, s22, 0x20800
	s_addc_u32 s23, s23, 0
	s_add_i32 s24, s26, s36
	v_lshl_add_u64 v[160:161], s[22:23], 0, v[130:131]
	s_mov_b32 m0, s24
	s_nop 0
	global_load_lds_dwordx4 v[160:161], off nt
	v_lshl_add_u64 v[160:161], s[22:23], 0, v[132:133]
	s_add_i32 m0, s24, 0x2000
	s_nop 0
	global_load_lds_dwordx4 v[160:161], off nt
	s_cmp_eq_u32 s82, 0
	s_cbranch_scc1 .Lpb8_p8n
	s_waitcnt vmcnt(14)
	s_branch .Lpb8_p8j

; __device__ __forceinline__ unsigned cvt_pk_bf16(float lo, float hi) { unsigned r; asm volatile("v_cvt_pk_bf16_f32 %0, %1, %2" : "=v"(r) : "v"(lo), "v"(hi)); return r; }
; #define PG8_STAGE(bufoff, gbase, v0, v1) do { \
;         __builtin_amdgcn_global_load_lds((const unsigned*)((const char*)(gbase) + (v0)), (LAS unsigned*)(lds + (bufoff) + ldsw), 16, 0, 0); \
;         __builtin_amdgcn_global_load_lds((const unsigned*)((const char*)(gbase) + (v1)), (LAS unsigned*)(lds + (bufoff) + ldsw + 8192), 16, 0, 0); } while (0)
; #define PG8_LDA(dst, b, h) do { _Pragma("unroll") for (int m = 0; m < 4; ++m) _Pragma("unroll") for (int k = 0; k < 2; ++k) dst[m][k] = *(const LAS bf16x8*)(lds + PG8_SA(b, h) + aoff + m * 2048 + k * 1024); } while (0)
; #define PG8_WAIT_V(n) asm volatile("s_waitcnt vmcnt(" #n ")" ::: "memory")
; #define PG8_WAIT_L(n) asm volatile("s_waitcnt lgkmcnt(" #n ")" ::: "memory")
; template <class Epi, class Sched>
; __device__ __forceinline__ void gemm_phase(LAS unsigned char* lds, const int K, const Sched& S, const Epi& E) {
;     ...
;             PG8_LDB(B0, 0, 0); PG8_SCHED; PG8_LDA(At, 0, 0); PG8_STAGE(PG8_SA(1, 1), a1, c10, c11);
;             PG8_WAIT_L(8); PG8_BAR; PG8_WAIT_L(0); PG8_MMA(0, 0, At, B0); PG8_BAR; PG8_SCHED;
;             PG8_LDB(B1, 0, 1); PG8_STAGE(PG8_SB(0, 0), b2, voffB0, voffB1);
;             PG8_BAR; PG8_WAIT_L(0); PG8_MMA(0, 1, At, B1); PG8_BAR;
;             PG8_LDA(At, 0, 1); PG8_STAGE(PG8_SA(0, 0), a2, x00, x01);
;             PG8_BAR; PG8_WAIT_L(0); PG8_MMA(1, 0, At, B0); PG8_BAR; PG8_SCHED;
;             PG8_STAGE(PG8_SB(0, 1), b2 + hstep, voffB0, voffB1);
;             PG8_WAIT_V(6); PG8_BAR; PG8_MMA(1, 1, At, B1); PG8_BAR;
; template <int BANK, int WAITN> __device__ __forceinline__ void bg_finish1(BgState& b) {
;     ...
;     if (dst != nullptr) {
; #pragma unroll
;         for (int c = 0; c < 4; ++c) { u32x4 w;
;             w.x = cvt_pk_bf16(b.r[(BANK * 8 + 0) * 4 + c], b.r[(BANK * 8 + 1) * 4 + c]); w.y = cvt_pk_bf16(b.r[(BANK * 8 + 2) * 4 + c], b.r[(BANK * 8 + 3) * 4 + c]);
;             w.z = cvt_pk_bf16(b.r[(BANK * 8 + 4) * 4 + c], b.r[(BANK * 8 + 5) * 4 + c]); w.w = cvt_pk_bf16(b.r[(BANK * 8 + 6) * 4 + c], b.r[(BANK * 8 + 7) * 4 + c]);
;             bf16_t* dp = dst + (c & 1) * 512 + (c >> 1) * b.o2[BANK];
;             asm volatile("global_store_dwordx4 %0, %1, off\n\ts_nop 1" :: "v"(dp), "v"(w) : "memory"); }
.LBB0_1831:
	v_add_u32_e32 v139, s46, v149
	s_add_u32 s22, s0, s20
	ds_read_b128 v[160:163], v139
	ds_read_b128 v[164:167], v139 offset:1024
	ds_read_b128 v[168:171], v139 offset:2048
	ds_read_b128 v[172:175], v139 offset:3072
	s_addc_u32 s23, s1, s21
	s_add_u32 s24, s22, 0x34c30100
	s_addc_u32 s25, s23, 0
	s_cmpk_eq_i32 s20, 0xf00
	s_cselect_b64 vcc, -1, 0
	s_and_b64 s[22:23], vcc, exec
	v_cndmask_b32_e32 v134, v158, v156, vcc
	s_cselect_b32 s27, s3, s25
	s_cselect_b32 s26, s2, s24
	v_cndmask_b32_e32 v139, v138, v154, vcc
	s_cselect_b32 s23, s19, s15
	s_cselect_b32 s22, s18, s13
	v_cndmask_b32_e32 v224, v136, v155, vcc
	s_add_u32 s24, s22, 0x20000
	s_addc_u32 s25, s23, 0
	v_lshl_add_u64 v[208:209], v[144:145], 0, s[20:21]
	s_add_i32 m0, s37, 0xc000
	ds_read_b128 v[176:179], v151
	ds_read_b128 v[180:183], v151 offset:1024
	ds_read_b128 v[184:187], v151 offset:2048
	ds_read_b128 v[188:191], v151 offset:3072
	ds_read_b128 v[192:195], v151 offset:4096
	ds_read_b128 v[196:199], v151 offset:5120
	ds_read_b128 v[200:203], v151 offset:6144
	ds_read_b128 v[204:207], v151 offset:7168
	global_load_lds_dwordx4 v[208:209], off
	v_lshl_add_u64 v[208:209], v[142:143], 0, s[20:21]
	s_add_i32 m0, s37, 0xe000
	s_nop 0
	global_load_lds_dwordx4 v[208:209], off
	s_waitcnt lgkmcnt(8)
	s_barrier
	s_waitcnt lgkmcnt(0)
	s_setprio 1
	s_waitcnt lgkmcnt(0)
	v_mfma_f32_16x16x32_bf16 v[126:129], v[160:163], v[176:179], v[126:129]
	v_mfma_f32_16x16x32_bf16 v[122:125], v[168:171], v[176:179], v[122:125]
	v_mfma_f32_16x16x32_bf16 v[110:113], v[160:163], v[184:187], v[110:113]
	v_mfma_f32_16x16x32_bf16 v[106:109], v[168:171], v[184:187], v[106:109]
	v_mfma_f32_16x16x32_bf16 v[94:97], v[160:163], v[192:195], v[94:97]
	v_mfma_f32_16x16x32_bf16 v[90:93], v[168:171], v[192:195], v[90:93]
	v_mfma_f32_16x16x32_bf16 v[78:81], v[160:163], v[200:203], v[78:81]
	v_mfma_f32_16x16x32_bf16 v[74:77], v[168:171], v[200:203], v[74:77]
	v_mfma_f32_16x16x32_bf16 v[126:129], v[164:167], v[180:183], v[126:129]
	v_mfma_f32_16x16x32_bf16 v[122:125], v[172:175], v[180:183], v[122:125]
	v_mfma_f32_16x16x32_bf16 v[110:113], v[164:167], v[188:191], v[110:113]
	v_mfma_f32_16x16x32_bf16 v[106:109], v[172:175], v[188:191], v[106:109]
	v_mfma_f32_16x16x32_bf16 v[94:97], v[164:167], v[196:199], v[94:97]
	v_mfma_f32_16x16x32_bf16 v[90:93], v[172:175], v[196:199], v[90:93]
	v_mfma_f32_16x16x32_bf16 v[78:81], v[164:167], v[204:207], v[78:81]
	v_mfma_f32_16x16x32_bf16 v[74:77], v[172:175], v[204:207], v[74:77]
	s_setprio 0
	s_barrier
	s_add_i32 s54, s46, s36
	v_add_u32_e32 v141, s48, v149
	v_lshl_add_u64 v[226:227], s[22:23], 0, v[130:131]
	s_mov_b32 m0, s54
	ds_read_b128 v[208:211], v141
	ds_read_b128 v[212:215], v141 offset:1024
	ds_read_b128 v[216:219], v141 offset:2048
	ds_read_b128 v[220:223], v141 offset:3072
	global_load_lds_dwordx4 v[226:227], off nt
	v_lshl_add_u64 v[228:229], s[22:23], 0, v[132:133]
	s_add_i32 m0, s54, 0x2000
	s_nop 0
	global_load_lds_dwordx4 v[228:229], off nt
	s_barrier
	s_waitcnt lgkmcnt(0)
	s_setprio 1
	s_waitcnt lgkmcnt(0)
	v_mfma_f32_16x16x32_bf16 v[118:121], v[208:211], v[176:179], v[118:121]
	v_mfma_f32_16x16x32_bf16 v[114:117], v[216:219], v[176:179], v[114:117]
	v_mfma_f32_16x16x32_bf16 v[102:105], v[208:211], v[184:187], v[102:105]
	v_mfma_f32_16x16x32_bf16 v[98:101], v[216:219], v[184:187], v[98:101]
	v_mfma_f32_16x16x32_bf16 v[86:89], v[208:211], v[192:195], v[86:89]
	v_mfma_f32_16x16x32_bf16 v[82:85], v[216:219], v[192:195], v[82:85]
	v_mfma_f32_16x16x32_bf16 v[70:73], v[208:211], v[200:203], v[70:73]
	v_mfma_f32_16x16x32_bf16 v[66:69], v[216:219], v[200:203], v[66:69]
	v_mfma_f32_16x16x32_bf16 v[118:121], v[212:215], v[180:183], v[118:121]
	v_mfma_f32_16x16x32_bf16 v[114:117], v[220:223], v[180:183], v[114:117]
	v_mfma_f32_16x16x32_bf16 v[102:105], v[212:215], v[188:191], v[102:105]
	v_mfma_f32_16x16x32_bf16 v[98:101], v[220:223], v[188:191], v[98:101]
	v_mfma_f32_16x16x32_bf16 v[86:89], v[212:215], v[196:199], v[86:89]
	v_mfma_f32_16x16x32_bf16 v[82:85], v[220:223], v[196:199], v[82:85]
	v_mfma_f32_16x16x32_bf16 v[70:73], v[212:215], v[204:207], v[70:73]
	v_mfma_f32_16x16x32_bf16 v[66:69], v[220:223], v[204:207], v[66:69]
	s_setprio 0
	s_mov_b32 m0, s37
	s_barrier
	ds_read_b128 v[176:179], v151 offset:16384
	ds_read_b128 v[180:183], v151 offset:17408
	ds_read_b128 v[184:187], v151 offset:18432
	ds_read_b128 v[188:191], v151 offset:19456
	ds_read_b128 v[192:195], v151 offset:20480
	ds_read_b128 v[196:199], v151 offset:21504
	ds_read_b128 v[200:203], v151 offset:22528
	ds_read_b128 v[204:207], v151 offset:23552
	global_load_lds_dwordx4 v134, s[26:27]
	s_mov_b32 m0, s38
	v_mov_b32_e32 v225, v135
	global_load_lds_dwordx4 v224, s[26:27]
	s_barrier
	s_waitcnt lgkmcnt(0)
	v_lshl_add_u64 v[230:231], s[26:27], 0, v[134:135]
	v_lshl_add_u64 v[224:225], s[26:27], 0, v[224:225]
	s_setprio 1
	s_waitcnt lgkmcnt(0)
	v_mfma_f32_16x16x32_bf16 v[62:65], v[160:163], v[176:179], v[62:65]
	v_mfma_f32_16x16x32_bf16 v[58:61], v[168:171], v[176:179], v[58:61]
	v_mfma_f32_16x16x32_bf16 v[46:49], v[160:163], v[184:187], v[46:49]
	v_mfma_f32_16x16x32_bf16 v[42:45], v[168:171], v[184:187], v[42:45]
	v_mfma_f32_16x16x32_bf16 v[30:33], v[160:163], v[192:195], v[30:33]
	v_mfma_f32_16x16x32_bf16 v[26:29], v[168:171], v[192:195], v[26:29]
	v_mfma_f32_16x16x32_bf16 v[14:17], v[160:163], v[200:203], v[14:17]
	v_mfma_f32_16x16x32_bf16 v[10:13], v[168:171], v[200:203], v[10:13]
	v_mfma_f32_16x16x32_bf16 v[62:65], v[164:167], v[180:183], v[62:65]
	v_mfma_f32_16x16x32_bf16 v[58:61], v[172:175], v[180:183], v[58:61]
	v_mfma_f32_16x16x32_bf16 v[46:49], v[164:167], v[188:191], v[46:49]
	v_mfma_f32_16x16x32_bf16 v[42:45], v[172:175], v[188:191], v[42:45]
	v_mfma_f32_16x16x32_bf16 v[30:33], v[164:167], v[196:199], v[30:33]
	v_mfma_f32_16x16x32_bf16 v[26:29], v[172:175], v[196:199], v[26:29]
	v_mfma_f32_16x16x32_bf16 v[14:17], v[164:167], v[204:207], v[14:17]
	v_mfma_f32_16x16x32_bf16 v[10:13], v[172:175], v[204:207], v[10:13]
	s_setprio 0
	s_barrier
	s_add_i32 s54, s48, s36
	v_lshl_add_u64 v[160:161], v[226:227], 0, s[4:5]
	s_mov_b32 m0, s54
	s_nop 0
	global_load_lds_dwordx4 v[160:161], off nt
	v_lshl_add_u64 v[160:161], v[228:229], 0, s[4:5]
	s_add_i32 m0, s54, 0x2000
	s_nop 0
	global_load_lds_dwordx4 v[160:161], off nt
	s_cmp_eq_u32 s82, 0
	s_cbranch_scc1 .Lpb17_p4n
	s_waitcnt vmcnt(14)
	v_cvt_pk_bf16_f32 v244, v244, v245
	v_cvt_pk_bf16_f32 v245, v246, v247
	v_cvt_pk_bf16_f32 v246, v248, v249
	v_cvt_pk_bf16_f32 v247, v250, v251
	global_store_dwordx4 v253, v[244:247], s[78:79] nt
	s_mov_b32 s82, 0
	s_waitcnt vmcnt(7)
	s_branch .Lpb17_p4j

; #define PG8_STAGE(bufoff, gbase, v0, v1) do { \
;         __builtin_amdgcn_global_load_lds((const unsigned*)((const char*)(gbase) + (v0)), (LAS unsigned*)(lds + (bufoff) + ldsw), 16, 0, 0); \
;         __builtin_amdgcn_global_load_lds((const unsigned*)((const char*)(gbase) + (v1)), (LAS unsigned*)(lds + (bufoff) + ldsw + 8192), 16, 0, 0); } while (0)
; #define PG8_LDA(dst, b, h) do { _Pragma("unroll") for (int m = 0; m < 4; ++m) _Pragma("unroll") for (int k = 0; k < 2; ++k) dst[m][k] = *(const LAS bf16x8*)(lds + PG8_SA(b, h) + aoff + m * 2048 + k * 1024); } while (0)
; #define PG8_LDB(dst, b, h) do { _Pragma("unroll") for (int n = 0; n < 2; ++n) _Pragma("unroll") for (int k = 0; k < 2; ++k) dst[n][k] = *(const LAS bf16x8*)(lds + PG8_SB(b, h) + boff + n * 2048 + k * 1024); } while (0)
; #define PG8_MMA(ai, bj, At, Bt) do { __builtin_amdgcn_s_setprio(1); _Pragma("unroll") for (int m = 0; m < 4; ++m) _Pragma("unroll") for (int n = 0; n < 2; ++n) _Pragma("unroll") for (int k = 0; k < 2; ++k) \
;         acc[ai][bj][m][n] = __builtin_amdgcn_mfma_f32_16x16x32_bf16(Bt[n][k], At[m][k], acc[ai][bj][m][n], 0, 0, 0); __builtin_amdgcn_s_setprio(0); } while (0)
; #define PG8_WAIT_V(n) asm volatile("s_waitcnt vmcnt(" #n ")" ::: "memory")
; #define PG8_WAIT_L(n) asm volatile("s_waitcnt lgkmcnt(" #n ")" ::: "memory")
; #define PG8_BAR __builtin_amdgcn_s_barrier()
; #define PG8_SCHED __builtin_amdgcn_sched_barrier(0)
; template <class Epi, class Sched>
; __device__ __forceinline__ void gemm_phase(LAS unsigned char* lds, const int K, const Sched& S, const Epi& E) {
;     ...
;             PG8_WAIT_L(8); PG8_BAR; PG8_WAIT_L(0); PG8_MMA(0, 0, At, B0); PG8_BAR; PG8_SCHED;
;             PG8_LDB(B1, 1, 1); PG8_STAGE(PG8_SB(1, 0), b3, voffB0, voffB1);
;             PG8_BAR; PG8_WAIT_L(0); PG8_MMA(0, 1, At, B1); PG8_BAR;
;             PG8_LDA(At, 1, 1); PG8_STAGE(PG8_SA(1, 0), a3, x00, x01);
;             PG8_BAR; PG8_WAIT_L(0); PG8_MMA(1, 0, At, B0); PG8_BAR; PG8_SCHED;
;             PG8_STAGE(PG8_SB(1, 1), b3 + hstep, voffB0, voffB1);
;             PG8_WAIT_V(6); PG8_BAR; PG8_MMA(1, 1, At, B1); PG8_BAR;
.Lpb17_p5n:
	s_waitcnt lgkmcnt(8)
	s_barrier
	s_waitcnt lgkmcnt(0)
	s_setprio 1
	s_waitcnt lgkmcnt(0)
	v_mfma_f32_16x16x32_bf16 v[126:129], v[160:163], v[176:179], v[126:129]
	v_mfma_f32_16x16x32_bf16 v[122:125], v[168:171], v[176:179], v[122:125]
	v_mfma_f32_16x16x32_bf16 v[110:113], v[160:163], v[184:187], v[110:113]
	v_mfma_f32_16x16x32_bf16 v[106:109], v[168:171], v[184:187], v[106:109]
	v_mfma_f32_16x16x32_bf16 v[94:97], v[160:163], v[192:195], v[94:97]
	v_mfma_f32_16x16x32_bf16 v[90:93], v[168:171], v[192:195], v[90:93]
	v_mfma_f32_16x16x32_bf16 v[78:81], v[160:163], v[200:203], v[78:81]
	v_mfma_f32_16x16x32_bf16 v[74:77], v[168:171], v[200:203], v[74:77]
	v_mfma_f32_16x16x32_bf16 v[126:129], v[164:167], v[180:183], v[126:129]
	v_mfma_f32_16x16x32_bf16 v[122:125], v[172:175], v[180:183], v[122:125]
	v_mfma_f32_16x16x32_bf16 v[110:113], v[164:167], v[188:191], v[110:113]
	v_mfma_f32_16x16x32_bf16 v[106:109], v[172:175], v[188:191], v[106:109]
	v_mfma_f32_16x16x32_bf16 v[94:97], v[164:167], v[196:199], v[94:97]
	v_mfma_f32_16x16x32_bf16 v[90:93], v[172:175], v[196:199], v[90:93]
	v_mfma_f32_16x16x32_bf16 v[78:81], v[164:167], v[204:207], v[78:81]
	v_mfma_f32_16x16x32_bf16 v[74:77], v[172:175], v[204:207], v[74:77]
	s_setprio 0
	s_barrier
	s_add_i32 s26, 0, 0x1c000
	s_add_i32 s27, s54, s36
	v_add_u32_e32 v134, s26, v149
	v_lshl_add_u64 v[226:227], s[24:25], 0, v[130:131]
	s_mov_b32 m0, s27
	ds_read_b128 v[208:211], v134
	ds_read_b128 v[212:215], v134 offset:1024
	ds_read_b128 v[216:219], v134 offset:2048
	ds_read_b128 v[220:223], v134 offset:3072
	global_load_lds_dwordx4 v[226:227], off nt
	v_lshl_add_u64 v[226:227], s[24:25], 0, v[132:133]
	s_add_i32 m0, s27, 0x2000
	s_nop 0
	global_load_lds_dwordx4 v[226:227], off nt
	s_barrier
	s_waitcnt lgkmcnt(0)
	s_setprio 1
	s_waitcnt lgkmcnt(0)
	v_mfma_f32_16x16x32_bf16 v[118:121], v[208:211], v[176:179], v[118:121]
	v_mfma_f32_16x16x32_bf16 v[114:117], v[216:219], v[176:179], v[114:117]
	v_mfma_f32_16x16x32_bf16 v[102:105], v[208:211], v[184:187], v[102:105]
	v_mfma_f32_16x16x32_bf16 v[98:101], v[216:219], v[184:187], v[98:101]
	v_mfma_f32_16x16x32_bf16 v[86:89], v[208:211], v[192:195], v[86:89]
	v_mfma_f32_16x16x32_bf16 v[82:85], v[216:219], v[192:195], v[82:85]
	v_mfma_f32_16x16x32_bf16 v[70:73], v[208:211], v[200:203], v[70:73]
	v_mfma_f32_16x16x32_bf16 v[66:69], v[216:219], v[200:203], v[66:69]
	v_mfma_f32_16x16x32_bf16 v[118:121], v[212:215], v[180:183], v[118:121]
	v_mfma_f32_16x16x32_bf16 v[114:117], v[220:223], v[180:183], v[114:117]
	v_mfma_f32_16x16x32_bf16 v[102:105], v[212:215], v[188:191], v[102:105]
	v_mfma_f32_16x16x32_bf16 v[98:101], v[220:223], v[188:191], v[98:101]
	v_mfma_f32_16x16x32_bf16 v[86:89], v[212:215], v[196:199], v[86:89]
	v_mfma_f32_16x16x32_bf16 v[82:85], v[220:223], v[196:199], v[82:85]
	v_mfma_f32_16x16x32_bf16 v[70:73], v[212:215], v[204:207], v[70:73]
	v_mfma_f32_16x16x32_bf16 v[66:69], v[220:223], v[204:207], v[66:69]
	s_setprio 0
	s_mov_b32 m0, s43
	v_lshl_add_u64 v[226:227], v[230:231], 0, s[10:11]
	s_barrier
	ds_read_b128 v[176:179], v151 offset:49152
	ds_read_b128 v[180:183], v151 offset:50176
	ds_read_b128 v[184:187], v151 offset:51200
	ds_read_b128 v[188:191], v151 offset:52224
	ds_read_b128 v[192:195], v151 offset:53248
	ds_read_b128 v[196:199], v151 offset:54272
	ds_read_b128 v[200:203], v151 offset:55296
	ds_read_b128 v[204:207], v151 offset:56320
	global_load_lds_dwordx4 v[226:227], off
	v_lshl_add_u64 v[224:225], v[224:225], 0, s[10:11]
	s_mov_b32 m0, s44
	s_nop 0
	global_load_lds_dwordx4 v[224:225], off
	s_barrier
	s_waitcnt lgkmcnt(0)
	s_setprio 1
	s_waitcnt lgkmcnt(0)
	v_mfma_f32_16x16x32_bf16 v[62:65], v[160:163], v[176:179], v[62:65]
	v_mfma_f32_16x16x32_bf16 v[58:61], v[168:171], v[176:179], v[58:61]
	v_mfma_f32_16x16x32_bf16 v[46:49], v[160:163], v[184:187], v[46:49]
	v_mfma_f32_16x16x32_bf16 v[42:45], v[168:171], v[184:187], v[42:45]
	v_mfma_f32_16x16x32_bf16 v[30:33], v[160:163], v[192:195], v[30:33]
	v_mfma_f32_16x16x32_bf16 v[26:29], v[168:171], v[192:195], v[26:29]
	v_mfma_f32_16x16x32_bf16 v[14:17], v[160:163], v[200:203], v[14:17]
	v_mfma_f32_16x16x32_bf16 v[10:13], v[168:171], v[200:203], v[10:13]
	v_mfma_f32_16x16x32_bf16 v[62:65], v[164:167], v[180:183], v[62:65]
	v_mfma_f32_16x16x32_bf16 v[58:61], v[172:175], v[180:183], v[58:61]
	v_mfma_f32_16x16x32_bf16 v[46:49], v[164:167], v[188:191], v[46:49]
	v_mfma_f32_16x16x32_bf16 v[42:45], v[172:175], v[188:191], v[42:45]
	v_mfma_f32_16x16x32_bf16 v[30:33], v[164:167], v[196:199], v[30:33]
	v_mfma_f32_16x16x32_bf16 v[26:29], v[172:175], v[196:199], v[26:29]
	v_mfma_f32_16x16x32_bf16 v[14:17], v[164:167], v[204:207], v[14:17]
	v_mfma_f32_16x16x32_bf16 v[10:13], v[172:175], v[204:207], v[10:13]
	s_setprio 0
	s_barrier
	s_add_u32 s22, s22, 0x20800
	s_addc_u32 s23, s23, 0
	s_add_i32 s24, s26, s36
	v_lshl_add_u64 v[160:161], s[22:23], 0, v[130:131]
	s_mov_b32 m0, s24
	s_nop 0
	global_load_lds_dwordx4 v[160:161], off nt
	v_lshl_add_u64 v[160:161], s[22:23], 0, v[132:133]
	s_add_i32 m0, s24, 0x2000
	s_nop 0
	global_load_lds_dwordx4 v[160:161], off nt
	s_cmp_eq_u32 s82, 0
	s_cbranch_scc1 .Lpb17_p8n
	s_waitcnt vmcnt(14)
	s_branch .Lpb17_p8j
